# v61 + weight-conversion loops: the 8 per-row gain loads of a unit issued together (one wait) instead of serialized load/wait pairs
# speedup vs baseline: 1.0002x; 1.0002x over previous
.LBB0_1063:
	s_andn2_b64 vcc, exec, s[26:27]
	s_cbranch_vccnz .LBB0_1073
	s_mov_b64 s[8:9], s[58:59]
	s_load_dwordx2 s[30:31], s[8:9], 0x38
	s_add_i32 s26, s39, 0xf600
	s_lshl_b64 s[8:9], s[22:23], 2
	v_mov_b32_e32 v54, 1.0
	v_mov_b32_e32 v56, 1.0
	s_waitcnt lgkmcnt(0)
	s_add_u32 s36, s30, s8
	s_addc_u32 s37, s31, s9
	s_lshr_b32 s9, s26, 1
	s_and_b32 s9, s9, 0x7fc0
	s_and_b32 s8, s1, 0xfe0
	v_add_u32_e32 v52, s9, v55
	s_lshl_b32 s92, s8, 2
	v_ashrrev_i32_e32 v53, 31, v52
	v_lshl_add_u64 v[0:1], v[36:37], 0, s[92:93]
	v_lshlrev_b64 v[2:3], 14, v[52:53]
	v_lshl_add_u64 v[0:1], v[0:1], 0, v[2:3]
	s_mov_b32 s26, 0x20000
	v_add_co_u32_e32 v2, vcc, s26, v0
	s_mov_b32 s26, 0x40000
	s_nop 0
	v_addc_co_u32_e32 v3, vcc, 0, v1, vcc
	global_load_dwordx4 v[28:31], v[0:1], off nt
	global_load_dwordx4 v[24:27], v[2:3], off nt
	v_add_co_u32_e32 v2, vcc, s26, v0
	s_mov_b32 s26, 0x60000
	s_nop 0
	v_addc_co_u32_e32 v3, vcc, 0, v1, vcc
	v_add_co_u32_e32 v4, vcc, s26, v0
	s_mov_b32 s26, 0x80000
	s_nop 0
	v_addc_co_u32_e32 v5, vcc, 0, v1, vcc
	global_load_dwordx4 v[20:23], v[2:3], off nt
	global_load_dwordx4 v[16:19], v[4:5], off nt
	v_add_co_u32_e32 v2, vcc, s26, v0
	s_mov_b32 s26, 0xa0000
	s_nop 0
	v_addc_co_u32_e32 v3, vcc, 0, v1, vcc
	v_add_co_u32_e32 v4, vcc, s26, v0
	s_cmp_lg_u64 s[30:31], 0
	s_nop 0
	v_addc_co_u32_e32 v5, vcc, 0, v1, vcc
	global_load_dwordx4 v[12:15], v[2:3], off nt
	global_load_dwordx4 v[8:11], v[4:5], off nt
	v_add_co_u32_e32 v2, vcc, 0xc0000, v0
	s_cselect_b64 s[26:27], -1, 0
	s_nop 0
	v_addc_co_u32_e32 v3, vcc, 0, v1, vcc
	v_add_co_u32_e32 v0, vcc, 0xe0000, v0
	s_cmp_eq_u64 s[30:31], 0
	s_nop 0
	v_addc_co_u32_e32 v1, vcc, 0, v1, vcc
	global_load_dwordx4 v[4:7], v[2:3], off nt
	s_nop 0
	global_load_dwordx4 v[0:3], v[0:1], off nt
	v_lshl_add_u64 v[52:53], v[52:53], 2, s[36:37]
	s_cbranch_scc1 .LBB0_1066
	global_load_dword v80, v[52:53], off
	global_load_dword v81, v[52:53], off offset:32
	global_load_dword v82, v[52:53], off offset:64
	global_load_dword v83, v[52:53], off offset:96
	global_load_dword v84, v[52:53], off offset:128
	global_load_dword v85, v[52:53], off offset:160
	global_load_dword v86, v[52:53], off offset:192
	global_load_dword v87, v[52:53], off offset:224
	s_waitcnt vmcnt(0)
	v_mov_b32_e32 v56, v80
	v_pk_mul_f32 v[28:29], v[28:29], v[56:57] op_sel_hi:[1,0]
	v_pk_mul_f32 v[30:31], v[30:31], v[56:57] op_sel_hi:[1,0]
	v_mov_b32_e32 v56, v81
.LBB0_1066:
	v_add_u32_e32 v66, v57, v58
	s_waitcnt vmcnt(7)
	ds_write2_b32 v66, v28, v29 offset1:1
	ds_write2_b32 v66, v30, v31 offset0:2 offset1:3
	s_waitcnt vmcnt(0)
	v_pk_mul_f32 v[24:25], v[24:25], v[56:57] op_sel_hi:[1,0]
	v_add_u32_e32 v28, 0x420, v66
	ds_write2_b32 v28, v24, v25 offset1:1
	v_pk_mul_f32 v[24:25], v[26:27], v[56:57] op_sel_hi:[1,0]
	v_cndmask_b32_e64 v27, 0, 1, s[26:27]
	v_add_u32_e32 v26, 0x428, v66
	v_cmp_ne_u32_e64 s[36:37], 1, v27
	s_andn2_b64 vcc, exec, s[26:27]
	ds_write2_b32 v26, v24, v25 offset1:1
	s_cbranch_vccnz .LBB0_1068
	v_mov_b32_e32 v24, v82
	v_mov_b32_e32 v54, v83
	s_waitcnt vmcnt(1)
	v_pk_mul_f32 v[20:21], v[20:21], v[24:25] op_sel_hi:[1,0]
	v_pk_mul_f32 v[22:23], v[22:23], v[24:25] op_sel_hi:[1,0]
.LBB0_1068:
	v_add_u32_e32 v24, 0x840, v66
	ds_write2_b32 v24, v20, v21 offset1:1
	v_add_u32_e32 v20, 0x848, v66
	ds_write2_b32 v20, v22, v23 offset1:1
	s_waitcnt vmcnt(0)
	v_pk_mul_f32 v[16:17], v[16:17], v[54:55] op_sel_hi:[1,0]
	v_add_u32_e32 v20, 0xc60, v66
	ds_write2_b32 v20, v16, v17 offset1:1
	v_pk_mul_f32 v[16:17], v[18:19], v[54:55] op_sel_hi:[1,0]
	v_add_u32_e32 v18, 0xc68, v66
	ds_write2_b32 v18, v16, v17 offset1:1
	v_mov_b32_e32 v16, 1.0
	s_and_b64 vcc, exec, s[36:37]
	v_mov_b32_e32 v18, 1.0
	s_cbranch_vccnz .LBB0_1070
	v_mov_b32_e32 v18, v84
	s_waitcnt vmcnt(0)
	v_pk_mul_f32 v[12:13], v[12:13], v[18:19] op_sel_hi:[1,0]
	v_pk_mul_f32 v[14:15], v[14:15], v[18:19] op_sel_hi:[1,0]
	v_mov_b32_e32 v18, v85
.LBB0_1070:
	v_add_u32_e32 v17, v57, v63
	ds_write2_b32 v17, v12, v13 offset1:1
	ds_write2_b32 v17, v14, v15 offset0:2 offset1:3
	s_waitcnt vmcnt(0)
	v_pk_mul_f32 v[8:9], v[8:9], v[18:19] op_sel_hi:[1,0]
	v_add_u32_e32 v12, 0x420, v17
	ds_write2_b32 v12, v8, v9 offset1:1
	v_pk_mul_f32 v[8:9], v[10:11], v[18:19] op_sel_hi:[1,0]
	v_add_u32_e32 v10, 0x428, v17
	s_and_b64 vcc, exec, s[36:37]
	ds_write2_b32 v10, v8, v9 offset1:1
	s_cbranch_vccnz .LBB0_1072
	v_mov_b32_e32 v8, v86
	v_mov_b32_e32 v16, v87
	s_waitcnt vmcnt(1)
	v_pk_mul_f32 v[4:5], v[4:5], v[8:9] op_sel_hi:[1,0]
	v_pk_mul_f32 v[6:7], v[6:7], v[8:9] op_sel_hi:[1,0]

.LBB0_1080:
	s_andn2_b64 vcc, exec, s[26:27]
	s_cbranch_vccnz .LBB0_1057
	s_mov_b64 s[8:9], s[58:59]
	s_load_dwordx2 s[8:9], s[8:9], 0x28
	s_lshl_b64 s[26:27], s[22:23], 2
	s_mul_hi_i32 s30, s39, 0x2aaaaaab
	v_mov_b32_e32 v54, 1.0
	v_mov_b32_e32 v56, 1.0
	s_waitcnt lgkmcnt(0)
	s_add_u32 s36, s8, s26
	s_addc_u32 s37, s9, s27
	s_lshr_b32 s26, s30, 31
	s_ashr_i32 s27, s30, 4
	s_add_i32 s26, s27, s26
	s_lshl_b32 s30, s26, 6
	s_mulk_i32 s26, 0xf400
	s_add_i32 s26, s1, s26
	v_add_u32_e32 v52, s30, v55
	s_ashr_i32 s27, s26, 31
	v_lshl_add_u64 v[0:1], s[26:27], 2, v[48:49]
	s_movk_i32 s27, 0x3000
	v_add_u32_e32 v4, 8, v52
	v_mad_i64_i32 v[2:3], s[40:41], v52, s27, v[0:1]
	v_mad_i64_i32 v[4:5], s[40:41], v4, s27, v[0:1]
	global_load_dwordx4 v[28:31], v[2:3], off nt
	global_load_dwordx4 v[24:27], v[4:5], off nt
	v_add_u32_e32 v2, 16, v52
	v_add_u32_e32 v4, 24, v52
	v_mad_i64_i32 v[2:3], s[40:41], v2, s27, v[0:1]
	v_mad_i64_i32 v[4:5], s[40:41], v4, s27, v[0:1]
	global_load_dwordx4 v[20:23], v[2:3], off nt
	global_load_dwordx4 v[16:19], v[4:5], off nt
	v_add_u32_e32 v2, 32, v52
	v_add_u32_e32 v4, 40, v52
	v_mad_i64_i32 v[2:3], s[40:41], v2, s27, v[0:1]
	v_mad_i64_i32 v[4:5], s[40:41], v4, s27, v[0:1]
	global_load_dwordx4 v[12:15], v[2:3], off nt
	global_load_dwordx4 v[8:11], v[4:5], off nt
	v_add_u32_e32 v2, 48, v52
	v_add_u32_e32 v4, 56, v52
	v_mad_i64_i32 v[2:3], s[40:41], v2, s27, v[0:1]
	v_mad_i64_i32 v[0:1], s[40:41], v4, s27, v[0:1]
	global_load_dwordx4 v[4:7], v[2:3], off nt
	s_nop 0
	global_load_dwordx4 v[0:3], v[0:1], off nt
	v_ashrrev_i32_e32 v53, 31, v52
	s_cmp_lg_u64 s[8:9], 0
	s_cselect_b64 s[40:41], -1, 0
	s_cmp_eq_u64 s[8:9], 0
	v_lshl_add_u64 v[52:53], v[52:53], 2, s[36:37]
	s_cbranch_scc1 .LBB0_1083
	global_load_dword v80, v[52:53], off
	global_load_dword v81, v[52:53], off offset:32
	global_load_dword v82, v[52:53], off offset:64
	global_load_dword v83, v[52:53], off offset:96
	global_load_dword v84, v[52:53], off offset:128
	global_load_dword v85, v[52:53], off offset:160
	global_load_dword v86, v[52:53], off offset:192
	global_load_dword v87, v[52:53], off offset:224
	s_waitcnt vmcnt(0)
	v_mov_b32_e32 v56, v80
	v_pk_mul_f32 v[28:29], v[28:29], v[56:57] op_sel_hi:[1,0]
	v_pk_mul_f32 v[30:31], v[30:31], v[56:57] op_sel_hi:[1,0]
	v_mov_b32_e32 v56, v81
.LBB0_1083:
	v_add_u32_e32 v66, v57, v58
	s_waitcnt vmcnt(7)
	ds_write2_b32 v66, v28, v29 offset1:1
	ds_write2_b32 v66, v30, v31 offset0:2 offset1:3
	s_waitcnt vmcnt(0)
	v_pk_mul_f32 v[24:25], v[24:25], v[56:57] op_sel_hi:[1,0]
	v_add_u32_e32 v28, 0x420, v66
	ds_write2_b32 v28, v24, v25 offset1:1
	v_pk_mul_f32 v[24:25], v[26:27], v[56:57] op_sel_hi:[1,0]
	v_cndmask_b32_e64 v27, 0, 1, s[40:41]
	v_add_u32_e32 v26, 0x428, v66
	v_cmp_ne_u32_e64 s[36:37], 1, v27
	s_andn2_b64 vcc, exec, s[40:41]
	ds_write2_b32 v26, v24, v25 offset1:1
	s_cbranch_vccnz .LBB0_1085
	v_mov_b32_e32 v24, v82
	v_mov_b32_e32 v54, v83
	s_waitcnt vmcnt(1)
	v_pk_mul_f32 v[20:21], v[20:21], v[24:25] op_sel_hi:[1,0]
	v_pk_mul_f32 v[22:23], v[22:23], v[24:25] op_sel_hi:[1,0]

.LBB0_1087:
	v_add_u32_e32 v17, v57, v63
	ds_write2_b32 v17, v12, v13 offset1:1
	ds_write2_b32 v17, v14, v15 offset0:2 offset1:3
	s_waitcnt vmcnt(0)
	v_pk_mul_f32 v[8:9], v[8:9], v[18:19] op_sel_hi:[1,0]
	v_add_u32_e32 v12, 0x420, v17
	ds_write2_b32 v12, v8, v9 offset1:1
	v_pk_mul_f32 v[8:9], v[10:11], v[18:19] op_sel_hi:[1,0]
	v_add_u32_e32 v10, 0x428, v17
	s_and_b64 vcc, exec, s[36:37]
	ds_write2_b32 v10, v8, v9 offset1:1
	s_cbranch_vccnz .LBB0_1056
	v_mov_b32_e32 v8, v86
	v_mov_b32_e32 v16, v87
	s_waitcnt vmcnt(1)
	v_pk_mul_f32 v[4:5], v[4:5], v[8:9] op_sel_hi:[1,0]
	v_pk_mul_f32 v[6:7], v[6:7], v[8:9] op_sel_hi:[1,0]
	s_branch .LBB0_1056

.LBB0_1104:
	s_andn2_b64 vcc, exec, s[26:27]
	s_cbranch_vccnz .LBB0_1114
	s_mov_b64 s[8:9], s[58:59]
	s_load_dwordx2 s[30:31], s[8:9], 0x38
	s_add_i32 s26, s1, 0xf600
	s_lshl_b64 s[8:9], s[22:23], 2
	v_mov_b32_e32 v54, 1.0
	v_mov_b32_e32 v56, 1.0
	s_waitcnt lgkmcnt(0)
	s_add_u32 s36, s30, s8
	s_addc_u32 s37, s31, s9
	s_lshr_b32 s9, s26, 1
	s_and_b32 s9, s9, 0x7fc0
	s_and_b32 s8, s33, 0xfe0
	v_add_u32_e32 v52, s9, v55
	s_lshl_b32 s92, s8, 2
	v_ashrrev_i32_e32 v53, 31, v52
	v_lshl_add_u64 v[0:1], v[36:37], 0, s[92:93]
	v_lshlrev_b64 v[2:3], 14, v[52:53]
	v_lshl_add_u64 v[0:1], v[0:1], 0, v[2:3]
	s_mov_b32 s26, 0x20000
	v_add_co_u32_e32 v2, vcc, s26, v0
	s_mov_b32 s26, 0x40000
	s_nop 0
	v_addc_co_u32_e32 v3, vcc, 0, v1, vcc
	global_load_dwordx4 v[28:31], v[0:1], off nt
	global_load_dwordx4 v[24:27], v[2:3], off nt
	v_add_co_u32_e32 v2, vcc, s26, v0
	s_mov_b32 s26, 0x60000
	s_nop 0
	v_addc_co_u32_e32 v3, vcc, 0, v1, vcc
	v_add_co_u32_e32 v4, vcc, s26, v0
	s_mov_b32 s26, 0x80000
	s_nop 0
	v_addc_co_u32_e32 v5, vcc, 0, v1, vcc
	global_load_dwordx4 v[20:23], v[2:3], off nt
	global_load_dwordx4 v[16:19], v[4:5], off nt
	v_add_co_u32_e32 v2, vcc, s26, v0
	s_mov_b32 s26, 0xa0000
	s_nop 0
	v_addc_co_u32_e32 v3, vcc, 0, v1, vcc
	v_add_co_u32_e32 v4, vcc, s26, v0
	s_cmp_lg_u64 s[30:31], 0
	s_nop 0
	v_addc_co_u32_e32 v5, vcc, 0, v1, vcc
	global_load_dwordx4 v[12:15], v[2:3], off nt
	global_load_dwordx4 v[8:11], v[4:5], off nt
	v_add_co_u32_e32 v2, vcc, 0xc0000, v0
	s_cselect_b64 s[26:27], -1, 0
	s_nop 0
	v_addc_co_u32_e32 v3, vcc, 0, v1, vcc
	v_add_co_u32_e32 v0, vcc, 0xe0000, v0
	s_cmp_eq_u64 s[30:31], 0
	s_nop 0
	v_addc_co_u32_e32 v1, vcc, 0, v1, vcc
	global_load_dwordx4 v[4:7], v[2:3], off nt
	s_nop 0
	global_load_dwordx4 v[0:3], v[0:1], off nt
	v_lshl_add_u64 v[52:53], v[52:53], 2, s[36:37]
	s_cbranch_scc1 .LBB0_1107
	global_load_dword v80, v[52:53], off
	global_load_dword v81, v[52:53], off offset:32
	global_load_dword v82, v[52:53], off offset:64
	global_load_dword v83, v[52:53], off offset:96
	global_load_dword v84, v[52:53], off offset:128
	global_load_dword v85, v[52:53], off offset:160
	global_load_dword v86, v[52:53], off offset:192
	global_load_dword v87, v[52:53], off offset:224
	s_waitcnt vmcnt(0)
	v_mov_b32_e32 v56, v80
	v_pk_mul_f32 v[28:29], v[28:29], v[56:57] op_sel_hi:[1,0]
	v_pk_mul_f32 v[30:31], v[30:31], v[56:57] op_sel_hi:[1,0]
	v_mov_b32_e32 v56, v81
.LBB0_1107:
	v_add_u32_e32 v64, v57, v58
	s_waitcnt vmcnt(7)
	ds_write2_b32 v64, v28, v29 offset1:1
	ds_write2_b32 v64, v30, v31 offset0:2 offset1:3
	s_waitcnt vmcnt(0)
	v_pk_mul_f32 v[24:25], v[24:25], v[56:57] op_sel_hi:[1,0]
	v_add_u32_e32 v28, 0x420, v64
	ds_write2_b32 v28, v24, v25 offset1:1
	v_pk_mul_f32 v[24:25], v[26:27], v[56:57] op_sel_hi:[1,0]
	v_cndmask_b32_e64 v27, 0, 1, s[26:27]
	v_add_u32_e32 v26, 0x428, v64
	v_cmp_ne_u32_e64 s[36:37], 1, v27
	s_andn2_b64 vcc, exec, s[26:27]
	ds_write2_b32 v26, v24, v25 offset1:1
	s_cbranch_vccnz .LBB0_1109
	v_mov_b32_e32 v24, v82
	v_mov_b32_e32 v54, v83
	s_waitcnt vmcnt(1)
	v_pk_mul_f32 v[20:21], v[20:21], v[24:25] op_sel_hi:[1,0]
	v_pk_mul_f32 v[22:23], v[22:23], v[24:25] op_sel_hi:[1,0]
.LBB0_1109:
	v_add_u32_e32 v24, 0x840, v64
	ds_write2_b32 v24, v20, v21 offset1:1
	v_add_u32_e32 v20, 0x848, v64
	ds_write2_b32 v20, v22, v23 offset1:1
	s_waitcnt vmcnt(0)
	v_pk_mul_f32 v[16:17], v[16:17], v[54:55] op_sel_hi:[1,0]
	v_add_u32_e32 v20, 0xc60, v64
	ds_write2_b32 v20, v16, v17 offset1:1
	v_pk_mul_f32 v[16:17], v[18:19], v[54:55] op_sel_hi:[1,0]
	v_add_u32_e32 v18, 0xc68, v64
	ds_write2_b32 v18, v16, v17 offset1:1
	v_mov_b32_e32 v16, 1.0
	s_and_b64 vcc, exec, s[36:37]
	v_mov_b32_e32 v18, 1.0
	s_cbranch_vccnz .LBB0_1111
	v_mov_b32_e32 v18, v84
	s_waitcnt vmcnt(0)
	v_pk_mul_f32 v[12:13], v[12:13], v[18:19] op_sel_hi:[1,0]
	v_pk_mul_f32 v[14:15], v[14:15], v[18:19] op_sel_hi:[1,0]
	v_mov_b32_e32 v18, v85

.LBB0_1121:
	s_andn2_b64 vcc, exec, s[26:27]
	s_cbranch_vccnz .LBB0_1098
	s_mov_b64 s[8:9], s[58:59]
	s_load_dwordx2 s[8:9], s[8:9], 0x28
	s_lshl_b64 s[26:27], s[22:23], 2
	s_mul_hi_i32 s30, s1, 0x2aaaaaab
	v_mov_b32_e32 v54, 1.0
	v_mov_b32_e32 v56, 1.0
	s_waitcnt lgkmcnt(0)
	s_add_u32 s36, s8, s26
	s_addc_u32 s37, s9, s27
	s_lshr_b32 s26, s30, 31
	s_ashr_i32 s27, s30, 4
	s_add_i32 s26, s27, s26
	s_lshl_b32 s30, s26, 6
	s_mulk_i32 s26, 0xf400
	s_add_i32 s26, s33, s26
	v_add_u32_e32 v52, s30, v55
	s_ashr_i32 s27, s26, 31
	v_lshl_add_u64 v[0:1], s[26:27], 2, v[48:49]
	s_movk_i32 s27, 0x3000
	v_add_u32_e32 v4, 8, v52
	v_mad_i64_i32 v[2:3], s[40:41], v52, s27, v[0:1]
	v_mad_i64_i32 v[4:5], s[40:41], v4, s27, v[0:1]
	global_load_dwordx4 v[28:31], v[2:3], off nt
	global_load_dwordx4 v[24:27], v[4:5], off nt
	v_add_u32_e32 v2, 16, v52
	v_add_u32_e32 v4, 24, v52
	v_mad_i64_i32 v[2:3], s[40:41], v2, s27, v[0:1]
	v_mad_i64_i32 v[4:5], s[40:41], v4, s27, v[0:1]
	global_load_dwordx4 v[20:23], v[2:3], off nt
	global_load_dwordx4 v[16:19], v[4:5], off nt
	v_add_u32_e32 v2, 32, v52
	v_add_u32_e32 v4, 40, v52
	v_mad_i64_i32 v[2:3], s[40:41], v2, s27, v[0:1]
	v_mad_i64_i32 v[4:5], s[40:41], v4, s27, v[0:1]
	global_load_dwordx4 v[12:15], v[2:3], off nt
	global_load_dwordx4 v[8:11], v[4:5], off nt
	v_add_u32_e32 v2, 48, v52
	v_add_u32_e32 v4, 56, v52
	v_mad_i64_i32 v[2:3], s[40:41], v2, s27, v[0:1]
	v_mad_i64_i32 v[0:1], s[40:41], v4, s27, v[0:1]
	global_load_dwordx4 v[4:7], v[2:3], off nt
	s_nop 0
	global_load_dwordx4 v[0:3], v[0:1], off nt
	v_ashrrev_i32_e32 v53, 31, v52
	s_cmp_lg_u64 s[8:9], 0
	s_cselect_b64 s[40:41], -1, 0
	s_cmp_eq_u64 s[8:9], 0
	v_lshl_add_u64 v[52:53], v[52:53], 2, s[36:37]
	s_cbranch_scc1 .LBB0_1124
	global_load_dword v80, v[52:53], off
	global_load_dword v81, v[52:53], off offset:32
	global_load_dword v82, v[52:53], off offset:64
	global_load_dword v83, v[52:53], off offset:96
	global_load_dword v84, v[52:53], off offset:128
	global_load_dword v85, v[52:53], off offset:160
	global_load_dword v86, v[52:53], off offset:192
	global_load_dword v87, v[52:53], off offset:224
	s_waitcnt vmcnt(0)
	v_mov_b32_e32 v56, v80
	v_pk_mul_f32 v[28:29], v[28:29], v[56:57] op_sel_hi:[1,0]
	v_pk_mul_f32 v[30:31], v[30:31], v[56:57] op_sel_hi:[1,0]
	v_mov_b32_e32 v56, v81
.LBB0_1124:
	v_add_u32_e32 v64, v57, v58
	s_waitcnt vmcnt(7)
	ds_write2_b32 v64, v28, v29 offset1:1
	ds_write2_b32 v64, v30, v31 offset0:2 offset1:3
	s_waitcnt vmcnt(0)
	v_pk_mul_f32 v[24:25], v[24:25], v[56:57] op_sel_hi:[1,0]
	v_add_u32_e32 v28, 0x420, v64
	ds_write2_b32 v28, v24, v25 offset1:1
	v_pk_mul_f32 v[24:25], v[26:27], v[56:57] op_sel_hi:[1,0]
	v_cndmask_b32_e64 v27, 0, 1, s[40:41]
	v_add_u32_e32 v26, 0x428, v64
	v_cmp_ne_u32_e64 s[36:37], 1, v27
	s_andn2_b64 vcc, exec, s[40:41]
	ds_write2_b32 v26, v24, v25 offset1:1
	s_cbranch_vccnz .LBB0_1126
	v_mov_b32_e32 v24, v82
	v_mov_b32_e32 v54, v83
	s_waitcnt vmcnt(1)
	v_pk_mul_f32 v[20:21], v[20:21], v[24:25] op_sel_hi:[1,0]
	v_pk_mul_f32 v[22:23], v[22:23], v[24:25] op_sel_hi:[1,0]
